# v039 + mLSTM scan: each workgroup walks its items last-first, so the one-wave normaliser item runs while the other waves already stream the state item
# speedup vs baseline: 1.0074x; 1.0028x over previous
; __device__ __forceinline__ int otid() { int t = threadIdx.x; asm volatile("" : "+v"(t)); return t; }
; __device__ __forceinline__ void phase_m2(const Ptrs& P, int tid_, int vcu, int G) {
;     const int tid = otid(); (void)tid_;
;     const float* cloc = (const float*)(P.ws + WS_CLOC); bf16* cprev = (bf16*)(P.ws + WS_CPREV);
;     float* sm = (float*)(P.ws + WS_SMALL); const float* nloc = sm; float* nprev = sm + 65536; const float* mg = sm + 131072; float* mprev = sm + 131072 + 2048;
;     for (int it = vcu; it < 64 * 5; it += G) {
;         const int small = it >= 256, seq = small ? it - 256 : it >> 2, blk = it & 3, dir = seq >> 5, bh = seq & 31;
;         if (small && tid >= 64) continue;
.Lm2_last_item:
	s_add_i32 s5, s4, s68
	s_cmpk_lt_i32 s5, 0x140
	s_cbranch_scc0 .LBB0_534
	s_mov_b32 s4, s5
	s_add_i32 s75, s75, s24
	s_branch .Lm2_last_item
.LBB0_533:
	s_or_b64 exec, exec, s[6:7]
	s_cmp_lt_i32 s4, s68
	s_cbranch_scc1 .LBB0_690
	s_sub_i32 s4, s4, s68
	s_sub_i32 s75, s75, s24
